# layer-0 norm_mix: f32 x rows +8/+16 of each wave prefetched into two 32-VGPR banks (on top of bf16 row banks and scaled fp8 convert)
# speedup vs baseline: 1.0033x; 1.0033x over previous
.LBB0_604:
	s_mov_b32 s101, 0
	s_xor_b64 s[12:13], s[4:5], -1
	s_add_u32 s6, s0, 0x33000000
	v_cndmask_b32_e64 v2, 0, 1, s[12:13]
	v_and_b32_e32 v222, 63, v197
	s_addc_u32 s7, s1, 0
	v_cmp_ne_u32_e64 s[38:39], 1, v2
	s_andn2_b64 vcc, exec, s[12:13]
	s_mov_b64 s[12:13], -1
	s_cbranch_vccnz .LBB0_610
	s_mul_hi_i32 s11, s10, 0x78787879
	s_lshr_b32 s12, s11, 31
	s_ashr_i32 s11, s11, 11
	s_add_i32 s11, s11, s12
	s_mul_i32 s12, s11, 0x1100
	s_sub_i32 s13, s10, s12
	s_add_u32 s14, s8, 16
	s_addc_u32 s15, s9, 0
	s_cmpk_gt_i32 s13, 0xff
	s_cbranch_scc0 .LBB0_607
	s_lshl_b32 s12, s11, 12
	s_add_i32 s12, s13, s12
	s_addk_i32 s12, 0xff00
	s_mov_b64 s[14:15], s[8:9]
	s_cbranch_execz .LBB0_608
	s_branch .LBB0_609

; template <bool ROUTER, bool SMALLP>
; __device__ __forceinline__ void norm_phase(KA A, LAS unsigned char* lds, int l, int which, int npart, const float* pgate, int tid, int wave, int lane, int bid) {
;     ...
;     f32x4 vnx[8]; v4u vnb[4]; bool nb;
;     NORM_LOAD(wave);
.LBB0_609:
	s_load_dwordx2 s[14:15], s[14:15], 0x0
	s_ashr_i32 s13, s12, 31
	s_lshl_b64 s[12:13], s[12:13], 13
	v_lshlrev_b32_e32 v14, 5, v222
	v_mov_b32_e32 v15, v130
	s_waitcnt lgkmcnt(0)
	s_add_u32 s12, s14, s12
	s_addc_u32 s13, s15, s13
	v_lshl_add_u64 v[26:27], s[12:13], 0, v[14:15]
	v_mov_b64_e32 v[114:115], v[26:27]
	global_load_dwordx4 v[2:5], v14, s[12:13] offset:16
	global_load_dwordx4 v[6:9], v14, s[12:13]
	global_load_dwordx4 v[10:13], v14, s[12:13] offset:2064
	s_nop 0
	global_load_dwordx4 v[14:17], v14, s[12:13] offset:2048
	s_mov_b64 s[12:13], 0x1000
	s_movk_i32 s11, 0x1000
	v_lshl_add_u64 v[22:23], v[26:27], 0, s[12:13]
	v_add_co_u32_e32 v28, vcc, s11, v26
	s_mov_b64 s[12:13], 0x1800
	s_nop 0
	v_addc_co_u32_e32 v29, vcc, 0, v27, vcc
	v_lshl_add_u64 v[30:31], v[26:27], 0, s[12:13]
	global_load_dwordx4 v[18:21], v[28:29], off
	s_nop 0
	global_load_dwordx4 v[22:25], v[22:23], off offset:16
	s_nop 0
	global_load_dwordx4 v[26:29], v[28:29], off offset:2048
	s_nop 0
	global_load_dwordx4 v[30:33], v[30:31], off offset:16
	s_mov_b32 s101, 2
	s_mov_b64 s[12:13], 0x10000
	v_lshl_add_u64 v[114:115], v[114:115], 0, s[12:13]
	s_mov_b64 s[12:13], 0x1000
	v_lshl_add_u64 v[116:117], v[114:115], 0, s[12:13]
	global_load_dwordx4 v[132:135], v[114:115], off offset:16
	global_load_dwordx4 v[136:139], v[114:115], off
	global_load_dwordx4 v[140:143], v[114:115], off offset:2064
	global_load_dwordx4 v[144:147], v[114:115], off offset:2048
	global_load_dwordx4 v[148:151], v[116:117], off
	global_load_dwordx4 v[152:155], v[116:117], off offset:16
	global_load_dwordx4 v[156:159], v[116:117], off offset:2048
	global_load_dwordx4 v[160:163], v[116:117], off offset:2064
	s_mov_b64 s[12:13], 0x10000
	v_lshl_add_u64 v[114:115], v[114:115], 0, s[12:13]
	s_mov_b64 s[12:13], 0x1000
	v_lshl_add_u64 v[116:117], v[114:115], 0, s[12:13]
	global_load_dwordx4 v[164:167], v[114:115], off offset:16
	global_load_dwordx4 v[168:171], v[114:115], off
	global_load_dwordx4 v[172:175], v[114:115], off offset:2064
	global_load_dwordx4 v[176:179], v[114:115], off offset:2048
	global_load_dwordx4 v[180:183], v[116:117], off
	global_load_dwordx4 v[184:187], v[116:117], off offset:16
	global_load_dwordx4 v[188:191], v[116:117], off offset:2048
	global_load_dwordx4 v[192:195], v[116:117], off offset:2064
	s_mov_b64 s[12:13], 0
.LBB0_610:
	s_and_b64 vcc, exec, s[12:13]
	v_lshlrev_b32_e32 v50, 4, v222
	s_cbranch_vccz .LBB0_612
	s_ashr_i32 s11, s10, 31
	s_lshl_b64 s[10:11], s[10:11], 12
	s_add_u32 s10, s6, s10
	s_addc_u32 s11, s7, s11
	global_load_dwordx4 v[34:37], v50, s[10:11]
	global_load_dwordx4 v[38:41], v50, s[10:11] offset:1024
	global_load_dwordx4 v[42:45], v50, s[10:11] offset:2048
	global_load_dwordx4 v[46:49], v50, s[10:11] offset:3072
	s_mov_b32 s101, 1
	s_add_u32 s10, s10, 0x8000
	s_addc_u32 s11, s11, 0
	global_load_dwordx4 v[134:137], v50, s[10:11]
	global_load_dwordx4 v[138:141], v50, s[10:11] offset:1024
	global_load_dwordx4 v[142:145], v50, s[10:11] offset:2048
	global_load_dwordx4 v[146:149], v50, s[10:11] offset:3072
	s_add_u32 s10, s10, 0x8000
	s_addc_u32 s11, s11, 0
	global_load_dwordx4 v[150:153], v50, s[10:11]
	global_load_dwordx4 v[154:157], v50, s[10:11] offset:1024
	global_load_dwordx4 v[158:161], v50, s[10:11] offset:2048
	global_load_dwordx4 v[162:165], v50, s[10:11] offset:3072
	s_add_u32 s10, s10, 0x8000
	s_addc_u32 s11, s11, 0
	global_load_dwordx4 v[166:169], v50, s[10:11]
	global_load_dwordx4 v[170:173], v50, s[10:11] offset:1024
	global_load_dwordx4 v[174:177], v50, s[10:11] offset:2048
	global_load_dwordx4 v[178:181], v50, s[10:11] offset:3072

; __device__ __forceinline__ int wg_row(int bid, int rl) { if (rl < 32) return (bid >> 7) * TB + CTXL + 32 * (bid & 127) + rl; const int q = 2 * bid + (rl - 32); return (q >> 8) * TB + (q & 255); }
; template <bool ROUTER, bool SMALLP>
; __device__ __forceinline__ void norm_phase(KA A, LAS unsigned char* lds, int l, int which, int npart, const float* pgate, int tid, int wave, int lane, int bid) {
;     ...
;     for (int rl = wave; rl < 34; rl += NWAVES) {
;         const int row = wg_row(bid, rl), s = row % TB; const bool isctx = s < CTXL; const int b = row / TB;
;         f32x4 v[8]; float ss = 0.f;
;         if (nb) {
; #pragma unroll
;             for (int jj = 0; jj < 4; ++jj) { float f[8]; unpack8(vnb[jj], f); v[2 * jj] = (f32x4){f[0], f[1], f[2], f[3]}; v[2 * jj + 1] = (f32x4){f[4], f[5], f[6], f[7]}; }
;         } else {
; #pragma unroll
;             for (int j = 0; j < 8; ++j) v[j] = vnx[j];
;         }
.LBB0_622:
	s_cmp_eq_u32 s101, 2
	s_cbranch_scc1 .Lnbk_f32top_A
	s_cmp_lt_i32 s27, 32
	s_cselect_b32 vcc_lo, s101, 0
	s_cmp_lg_u32 vcc_lo, 0
	s_cbranch_scc0 .Lnbk_otop_A
	s_waitcnt vmcnt(12)
	s_branch .Lnbk_unpack_A
.Lnbk_f32top_A:
	s_cmp_lt_i32 s27, 24
	s_cbranch_scc0 .Lnbk_otop_A
	s_waitcnt vmcnt(16)
	v_mov_b64_e32 v[80:81], v[8:9]
	v_mov_b64_e32 v[72:73], v[4:5]
	v_mov_b64_e32 v[76:77], v[16:17]
	v_mov_b64_e32 v[64:65], v[12:13]
	v_mov_b64_e32 v[68:69], v[20:21]
	v_mov_b64_e32 v[56:57], v[24:25]
	v_mov_b64_e32 v[60:61], v[28:29]
	v_mov_b64_e32 v[52:53], v[32:33]
	v_mov_b64_e32 v[78:79], v[6:7]
	v_mov_b64_e32 v[70:71], v[2:3]
	v_mov_b64_e32 v[74:75], v[14:15]
	v_mov_b64_e32 v[62:63], v[10:11]
	v_mov_b64_e32 v[66:67], v[18:19]
	v_mov_b64_e32 v[54:55], v[22:23]
	v_mov_b64_e32 v[58:59], v[26:27]
	v_mov_b64_e32 v[50:51], v[30:31]
	s_branch .LBB0_624

; template <bool ROUTER, bool SMALLP>
; __device__ __forceinline__ void norm_phase(KA A, LAS unsigned char* lds, int l, int which, int npart, const float* pgate, int tid, int wave, int lane, int bid) {
;     ...
;         if (rl + NWAVES < 34) NORM_LOAD(rl + NWAVES);
.LBB0_624:
	s_cmp_gt_i32 s27, 25
	s_cselect_b64 s[22:23], -1, 0
	s_and_b64 vcc, exec, s[22:23]
	s_cbranch_vccnz .LBB0_638
	s_cmp_eq_u32 s101, 2
	s_cbranch_scc1 .Lnbk_f32mid_A
	s_cmp_lt_i32 s27, 24
	s_cselect_b32 vcc_lo, s101, 0
	s_cmp_lg_u32 vcc_lo, 0
	s_cbranch_scc0 .Lnbk_omid_A
	s_waitcnt vmcnt(8)
	s_cmp_gt_i32 s27, 7
	s_cbranch_scc1 .Lnbk_b2_A
	v_mov_b64_e32 v[34:35], v[134:135]
	v_mov_b64_e32 v[36:37], v[136:137]
	v_mov_b64_e32 v[38:39], v[138:139]
	v_mov_b64_e32 v[40:41], v[140:141]
	v_mov_b64_e32 v[42:43], v[142:143]
	v_mov_b64_e32 v[44:45], v[144:145]
	v_mov_b64_e32 v[46:47], v[146:147]
	v_mov_b64_e32 v[48:49], v[148:149]
	s_branch .LBB0_638

; template <bool ROUTER, bool SMALLP>
; __device__ __forceinline__ void norm_phase(KA A, LAS unsigned char* lds, int l, int which, int npart, const float* pgate, int tid, int wave, int lane, int bid) {
;     ...
;         if (rl + NWAVES < 34) NORM_LOAD(rl + NWAVES);
.Lnbk_f32mid_A:
	s_cmp_lt_i32 s27, 16
	s_cbranch_scc0 .Lnbk_omid_A
	s_cmp_gt_i32 s27, 7
	s_cbranch_scc1 .Lnbk_f32b2_A
	s_waitcnt vmcnt(8)
	v_mov_b64_e32 v[2:3], v[132:133]
	v_mov_b64_e32 v[4:5], v[134:135]
	v_mov_b64_e32 v[6:7], v[136:137]
	v_mov_b64_e32 v[8:9], v[138:139]
	v_mov_b64_e32 v[10:11], v[140:141]
	v_mov_b64_e32 v[12:13], v[142:143]
	v_mov_b64_e32 v[14:15], v[144:145]
	v_mov_b64_e32 v[16:17], v[146:147]
	v_mov_b64_e32 v[18:19], v[148:149]
	v_mov_b64_e32 v[20:21], v[150:151]
	v_mov_b64_e32 v[22:23], v[152:153]
	v_mov_b64_e32 v[24:25], v[154:155]
	v_mov_b64_e32 v[26:27], v[156:157]
	v_mov_b64_e32 v[28:29], v[158:159]
	v_mov_b64_e32 v[30:31], v[160:161]
	v_mov_b64_e32 v[32:33], v[162:163]
	s_mov_b64 s[20:21], 0
	s_branch .LBB0_638
.Lnbk_f32b2_A:
	s_waitcnt vmcnt(4)
	v_mov_b64_e32 v[2:3], v[164:165]
	v_mov_b64_e32 v[4:5], v[166:167]
	v_mov_b64_e32 v[6:7], v[168:169]
	v_mov_b64_e32 v[8:9], v[170:171]
	v_mov_b64_e32 v[10:11], v[172:173]
	v_mov_b64_e32 v[12:13], v[174:175]
	v_mov_b64_e32 v[14:15], v[176:177]
	v_mov_b64_e32 v[16:17], v[178:179]
	v_mov_b64_e32 v[18:19], v[180:181]
	v_mov_b64_e32 v[20:21], v[182:183]
	v_mov_b64_e32 v[22:23], v[184:185]
	v_mov_b64_e32 v[24:25], v[186:187]
	v_mov_b64_e32 v[26:27], v[188:189]
	v_mov_b64_e32 v[28:29], v[190:191]
	v_mov_b64_e32 v[30:31], v[192:193]
	v_mov_b64_e32 v[32:33], v[194:195]
	s_mov_b64 s[20:21], 0
	s_branch .LBB0_638
